# baseline (speedup 1.0000x reference)
.LBB1_11:
	s_lshl_b32 s0, s30, 5
	s_lshl_b32 s1, s31, 7
	s_and_b32 s13, s2, 3
	s_or_b32 s14, s0, s1
	s_lshl_b32 s4, s28, 7
	s_lshl_b32 s5, s31, 2
	s_add_i32 s4, s4, s5
	s_add_i32 s4, s4, s30
	s_lshl_b32 s4, s4, 1
	s_add_i32 s4, s4, s3
	s_lshl_b32 s4, s4, 12
	s_add_u32 s4, s18, s4
	s_addc_u32 s5, s19, 0
	v_lshlrev_b32_e32 v0, 2, v173
	s_lshl_b32 s0, s3, 5
	s_lshl_b32 s12, s13, 6
	s_mov_b32 s1, 0
	s_mov_b32 s15, 0
	global_load_dwordx4 v[124:127], v0, s[4:5] nt
	global_load_dwordx4 v[128:131], v0, s[4:5] offset:1024 nt
	global_load_dwordx4 v[132:135], v0, s[4:5] offset:2048 nt
	global_load_dwordx4 v[136:139], v0, s[4:5] offset:3072 nt
	s_lshl_b64 s[2:3], s[14:15], 2
	v_mov_b32_e32 v37, 0
	v_lshlrev_b32_e32 v36, 2, v172
	v_lshlrev_b32_e32 v122, 16, v175
	v_mov_b32_e32 v123, 0
	s_mul_i32 s4, s29, 0x2200
	s_add_i32 s4, s4, 0
	v_mov_b32_e32 v8, v141
	v_add_u32_e32 v9, s4, v173
	s_xor_b32 s4, s29, 4
	v_permlane32_swap_b32_e32 v141, v8
	s_mulk_i32 s4, 0x2200
	v_add_f32_e32 v8, v141, v8
	s_add_i32 s4, s4, 0
	ds_write2st64_b32 v9, v146, v8 offset1:1
	ds_write2st64_b32 v9, v54, v55 offset0:2 offset1:3
	ds_write2st64_b32 v9, v38, v39 offset0:18 offset1:19
	ds_write2st64_b32 v9, v56, v57 offset0:4 offset1:5
	ds_write2st64_b32 v9, v40, v41 offset0:20 offset1:21
	ds_write2st64_b32 v9, v58, v59 offset0:6 offset1:7
	ds_write2st64_b32 v9, v42, v43 offset0:22 offset1:23
	ds_write2st64_b32 v9, v60, v61 offset0:8 offset1:9
	ds_write2st64_b32 v9, v44, v45 offset0:24 offset1:25
	ds_write2st64_b32 v9, v62, v63 offset0:10 offset1:11
	ds_write2st64_b32 v9, v46, v47 offset0:26 offset1:27
	ds_write2st64_b32 v9, v64, v65 offset0:12 offset1:13
	ds_write2st64_b32 v9, v48, v49 offset0:28 offset1:29
	ds_write2st64_b32 v9, v66, v67 offset0:14 offset1:15
	ds_write2st64_b32 v9, v50, v51 offset0:30 offset1:31
	ds_write2st64_b32 v9, v68, v69 offset0:16 offset1:17
	ds_write2st64_b32 v9, v52, v53 offset0:32 offset1:33
	v_add_u32_e32 v66, s4, v173
	s_waitcnt lgkmcnt(0)
	s_barrier
	ds_read2st64_b32 v[10:11], v66 offset1:1
	ds_read2st64_b32 v[12:13], v66 offset0:2 offset1:3
	ds_read2st64_b32 v[14:15], v66 offset0:4 offset1:5
	ds_read2st64_b32 v[38:39], v66 offset0:6 offset1:7
	v_max_f32_e32 v40, v146, v146
	s_waitcnt lgkmcnt(3)
	v_max_f32_e32 v9, v10, v10
	v_max_f32_e32 v9, v40, v9
	v_sub_f32_e32 v40, v146, v9
	v_sub_f32_e32 v9, v10, v9
	v_exp_f32_e32 v40, v40
	v_exp_f32_e32 v41, v9
	v_mov_b32_e32 v9, v11
	v_pk_mul_f32 v[8:9], v[8:9], v[40:41]
	s_nop 0
	v_add_f32_e32 v8, v8, v9
	v_div_scale_f32 v9, s[4:5], v8, v8, 1.0
	v_rcp_f32_e32 v10, v9
	s_nop 0
	v_fma_f32 v11, -v9, v10, 1.0
	v_fmac_f32_e32 v10, v11, v10
	v_div_scale_f32 v11, vcc, 1.0, v8, 1.0
	v_mul_f32_e32 v42, v11, v10
	v_fma_f32 v43, -v9, v42, v11
	v_fmac_f32_e32 v42, v43, v10
	v_fma_f32 v9, -v9, v42, v11
	v_div_fmas_f32 v9, v9, v10, v42
	v_div_fixup_f32 v9, v9, v8, 1.0
	v_mul_f32_e32 v8, v40, v9
	v_mul_f32_e32 v10, v41, v9
	ds_read2st64_b32 v[40:41], v66 offset0:18 offset1:19
	ds_read2st64_b32 v[42:43], v66 offset0:20 offset1:21
	ds_read2st64_b32 v[44:45], v66 offset0:22 offset1:23
	ds_read2st64_b32 v[46:47], v66 offset0:16 offset1:17
	s_waitcnt lgkmcnt(6)
	v_pk_mul_f32 v[12:13], v[10:11], v[12:13] op_sel_hi:[0,1]
	s_waitcnt lgkmcnt(5)
	v_pk_mul_f32 v[14:15], v[10:11], v[14:15] op_sel_hi:[0,1]
	s_waitcnt lgkmcnt(4)
	v_pk_mul_f32 v[38:39], v[10:11], v[38:39] op_sel_hi:[0,1]
	s_waitcnt lgkmcnt(3)
	v_pk_mul_f32 v[40:41], v[10:11], v[40:41] op_sel_hi:[0,1]
	v_pk_fma_f32 v[48:49], v[8:9], v[70:71], v[40:41] op_sel_hi:[0,1,1]
	s_waitcnt lgkmcnt(2)
	v_pk_mul_f32 v[40:41], v[10:11], v[42:43] op_sel_hi:[0,1]
	v_pk_fma_f32 v[50:51], v[8:9], v[72:73], v[40:41] op_sel_hi:[0,1,1]
	s_waitcnt lgkmcnt(1)
	v_pk_mul_f32 v[40:41], v[10:11], v[44:45] op_sel_hi:[0,1]
	v_pk_fma_f32 v[52:53], v[8:9], v[74:75], v[40:41] op_sel_hi:[0,1,1]
	ds_read2st64_b32 v[40:41], v66 offset0:8 offset1:9
	ds_read2st64_b32 v[42:43], v66 offset0:24 offset1:25
	ds_read2st64_b32 v[44:45], v66 offset0:10 offset1:11
	ds_read2st64_b32 v[54:55], v66 offset0:12 offset1:13
	ds_read2st64_b32 v[56:57], v66 offset0:14 offset1:15
	ds_read2st64_b32 v[58:59], v66 offset0:26 offset1:27
	ds_read2st64_b32 v[60:61], v66 offset0:28 offset1:29
	ds_read2st64_b32 v[62:63], v66 offset0:30 offset1:31
	s_waitcnt lgkmcnt(6)
	v_pk_mul_f32 v[42:43], v[10:11], v[42:43] op_sel_hi:[0,1]
	v_pk_fma_f32 v[64:65], v[8:9], v[76:77], v[42:43] op_sel_hi:[0,1,1]
	s_waitcnt lgkmcnt(5)
	v_pk_mul_f32 v[42:43], v[10:11], v[44:45] op_sel_hi:[0,1]
	s_waitcnt lgkmcnt(2)
	v_pk_mul_f32 v[44:45], v[10:11], v[58:59] op_sel_hi:[0,1]
	v_pk_fma_f32 v[58:59], v[8:9], v[78:79], v[44:45] op_sel_hi:[0,1,1]
	v_pk_mul_f32 v[44:45], v[10:11], v[54:55] op_sel_hi:[0,1]
	s_waitcnt lgkmcnt(1)
	v_pk_mul_f32 v[54:55], v[10:11], v[60:61] op_sel_hi:[0,1]
	ds_read2st64_b32 v[60:61], v66 offset0:32 offset1:33
	s_waitcnt vmcnt(0)
	v_pk_mul_f32 v[40:41], v[10:11], v[40:41] op_sel_hi:[0,1]
	v_cvt_pk_bf16_f32 v0, v208, v209
	v_cvt_pk_bf16_f32 v1, v210, v211
	v_cvt_pk_bf16_f32 v2, v212, v213
	v_cvt_pk_bf16_f32 v3, v214, v215
	v_pk_fma_f32 v[12:13], v[8:9], v[86:87], v[12:13] op_sel_hi:[0,1,1]
	v_pk_fma_f32 v[14:15], v[8:9], v[88:89], v[14:15] op_sel_hi:[0,1,1]
	v_pk_fma_f32 v[38:39], v[8:9], v[90:91], v[38:39] op_sel_hi:[0,1,1]
	v_pk_fma_f32 v[40:41], v[8:9], v[92:93], v[40:41] op_sel_hi:[0,1,1]
	v_pk_mul_f32 v[56:57], v[10:11], v[56:57] op_sel_hi:[0,1]
	s_waitcnt lgkmcnt(1)
	v_pk_mul_f32 v[62:63], v[10:11], v[62:63] op_sel_hi:[0,1]
	v_pk_mul_f32 v[46:47], v[10:11], v[46:47] op_sel_hi:[0,1]
	s_waitcnt lgkmcnt(0)
	v_pk_mul_f32 v[10:11], v[10:11], v[60:61] op_sel_hi:[0,1]
	v_cvt_pk_bf16_f32 v4, v12, v13
	v_cvt_pk_bf16_f32 v5, v14, v15
	v_cvt_pk_bf16_f32 v6, v38, v39
	v_cvt_pk_bf16_f32 v7, v40, v41
	v_pk_fma_f32 v[42:43], v[8:9], v[94:95], v[42:43] op_sel_hi:[0,1,1]
	v_pk_fma_f32 v[44:45], v[8:9], v[96:97], v[44:45] op_sel_hi:[0,1,1]
	v_pk_fma_f32 v[54:55], v[8:9], v[80:81], v[54:55] op_sel_hi:[0,1,1]
	v_pk_fma_f32 v[56:57], v[8:9], v[98:99], v[56:57] op_sel_hi:[0,1,1]
	v_pk_fma_f32 v[62:63], v[8:9], v[82:83], v[62:63] op_sel_hi:[0,1,1]
	v_pk_fma_f32 v[46:47], v[8:9], v[100:101], v[46:47] op_sel_hi:[0,1,1]
	v_pk_fma_f32 v[60:61], v[8:9], v[84:85], v[10:11] op_sel_hi:[0,1,1]
	v_mfma_f32_32x32x16_bf16 v[0:15], v[0:3], v[4:7], 0
	v_cvt_pk_bf16_f32 v42, v42, v43
	v_cvt_pk_bf16_f32 v38, v216, v217
	v_cvt_pk_bf16_f32 v39, v218, v219
	v_cvt_pk_bf16_f32 v40, v220, v221
	v_cvt_pk_bf16_f32 v41, v222, v223
	v_cvt_pk_bf16_f32 v43, v44, v45
	v_cvt_pk_bf16_f32 v44, v56, v57
	v_cvt_pk_bf16_f32 v45, v46, v47
	s_nop 1
	v_mfma_f32_32x32x16_bf16 v[0:15], v[38:41], v[42:45], v[0:15]
	v_cvt_pk_bf16_f32 v38, v224, v225
	v_cvt_pk_bf16_f32 v39, v226, v227
	v_cvt_pk_bf16_f32 v40, v228, v229
	v_cvt_pk_bf16_f32 v41, v230, v231
	v_cvt_pk_bf16_f32 v42, v48, v49
	v_cvt_pk_bf16_f32 v43, v50, v51
	v_cvt_pk_bf16_f32 v44, v52, v53
	v_cvt_pk_bf16_f32 v45, v64, v65
	v_cvt_pk_bf16_f32 v32, v232, v233
	v_cvt_pk_bf16_f32 v33, v234, v235
	v_mfma_f32_32x32x16_bf16 v[0:15], v[38:41], v[42:45], v[0:15]
	v_cvt_pk_bf16_f32 v34, v236, v237
	v_cvt_pk_bf16_f32 v35, v238, v239
	v_cvt_pk_bf16_f32 v38, v58, v59
	v_add_f32_e32 v42, 1.0, v205
	v_div_scale_f32 v43, s[4:5], v42, v42, 1.0
	v_rcp_f32_e32 v44, v43
	v_cvt_pk_bf16_f32 v39, v54, v55
	v_cvt_pk_bf16_f32 v40, v62, v63
	v_cvt_pk_bf16_f32 v41, v60, v61
	s_lshl_b32 s4, s28, 8
	s_or_b32 s4, s4, s12
	v_mfma_f32_32x32x16_bf16 v[0:15], v[32:35], v[38:41], v[0:15]
	v_fma_f32 v32, -v43, v44, 1.0
	v_fmac_f32_e32 v44, v32, v44
	v_div_scale_f32 v32, vcc, 1.0, v42, 1.0
	s_add_i32 s0, s4, s0
	v_mul_f32_e32 v33, v32, v44
	s_lshl_b64 s[0:1], s[0:1], 14
	v_fma_f32 v34, -v43, v33, v32
	s_add_u32 s0, s10, s0
	v_fmac_f32_e32 v33, v34, v44
	s_addc_u32 s1, s11, s1
	v_fma_f32 v32, -v43, v33, v32
	s_add_u32 s0, s0, s2
	v_div_fmas_f32 v32, v32, v44, v33
	s_addc_u32 s1, s1, s3
	v_add_f32_e32 v0, v0, v240
	v_div_fixup_f32 v34, v32, v42, 1.0
	v_lshl_add_u64 v[32:33], s[0:1], 0, v[36:37]
	v_fmac_f32_e32 v124, v205, v0
	v_mul_f32_e32 v0, v34, v124
	v_lshl_add_u64 v[32:33], v[32:33], 0, v[122:123]
	global_store_dword v[32:33], v0, off sc1
	v_add_f32_e32 v0, v1, v241
	s_movk_i32 s0, 0x4000
	v_fmac_f32_e32 v125, v205, v0
	v_add_co_u32_e32 v0, vcc, s0, v32
	v_mul_f32_e32 v28, v34, v125
	s_nop 0
	v_addc_co_u32_e32 v1, vcc, 0, v33, vcc
	global_store_dword v[0:1], v28, off sc1
	v_add_f32_e32 v0, v2, v242
	s_mov_b32 s0, 0x8000
	v_fmac_f32_e32 v126, v205, v0
	v_add_co_u32_e32 v0, vcc, s0, v32
	v_mul_f32_e32 v2, v34, v126
	s_nop 0
	v_addc_co_u32_e32 v1, vcc, 0, v33, vcc
	global_store_dword v[0:1], v2, off sc1
	v_add_f32_e32 v0, v3, v243
	s_mov_b32 s0, 0xc000
	v_fmac_f32_e32 v127, v205, v0
	v_add_co_u32_e32 v0, vcc, s0, v32
	v_mul_f32_e32 v2, v34, v127
	s_nop 0
	v_addc_co_u32_e32 v1, vcc, 0, v33, vcc
	global_store_dword v[0:1], v2, off sc1
	v_add_f32_e32 v0, v4, v244
	s_mov_b32 s0, 0x20000
	v_fmac_f32_e32 v128, v205, v0
	v_add_co_u32_e32 v0, vcc, s0, v32
	v_mul_f32_e32 v2, v34, v128
	s_nop 0
	v_addc_co_u32_e32 v1, vcc, 0, v33, vcc
	global_store_dword v[0:1], v2, off sc1
	v_add_f32_e32 v0, v5, v245
	s_mov_b32 s0, 0x24000
	v_fmac_f32_e32 v129, v205, v0
	v_add_co_u32_e32 v0, vcc, s0, v32
	v_mul_f32_e32 v2, v34, v129
	s_nop 0
	v_addc_co_u32_e32 v1, vcc, 0, v33, vcc
	global_store_dword v[0:1], v2, off sc1
	v_add_f32_e32 v0, v6, v246
	s_mov_b32 s0, 0x28000
	v_fmac_f32_e32 v130, v205, v0
	v_add_co_u32_e32 v0, vcc, s0, v32
	v_mul_f32_e32 v2, v34, v130
	s_nop 0
	v_addc_co_u32_e32 v1, vcc, 0, v33, vcc
	global_store_dword v[0:1], v2, off sc1
	v_add_f32_e32 v0, v7, v247
	s_mov_b32 s0, 0x2c000
	v_fmac_f32_e32 v131, v205, v0
	v_add_co_u32_e32 v0, vcc, s0, v32
	v_mul_f32_e32 v2, v34, v131
	s_nop 0
	v_addc_co_u32_e32 v1, vcc, 0, v33, vcc
	global_store_dword v[0:1], v2, off sc1
	v_add_f32_e32 v0, v8, v248
	s_mov_b32 s0, 0x40000
	v_fmac_f32_e32 v132, v205, v0
	v_add_co_u32_e32 v0, vcc, s0, v32
	v_mul_f32_e32 v2, v34, v132
	s_nop 0
	v_addc_co_u32_e32 v1, vcc, 0, v33, vcc
	global_store_dword v[0:1], v2, off sc1
	v_add_f32_e32 v0, v9, v249
	s_mov_b32 s0, 0x44000
	v_fmac_f32_e32 v133, v205, v0
	v_add_co_u32_e32 v0, vcc, s0, v32
	v_mul_f32_e32 v2, v34, v133
	s_nop 0
	v_addc_co_u32_e32 v1, vcc, 0, v33, vcc
	global_store_dword v[0:1], v2, off sc1
	v_add_f32_e32 v0, v10, v250
	s_mov_b32 s0, 0x48000
	v_fmac_f32_e32 v134, v205, v0
	v_add_co_u32_e32 v0, vcc, s0, v32
	v_mul_f32_e32 v2, v34, v134
	s_nop 0
	v_addc_co_u32_e32 v1, vcc, 0, v33, vcc
	global_store_dword v[0:1], v2, off sc1
	v_add_f32_e32 v0, v11, v251
	s_mov_b32 s0, 0x4c000
	v_fmac_f32_e32 v135, v205, v0
	v_add_co_u32_e32 v0, vcc, s0, v32
	v_mul_f32_e32 v2, v34, v135
	s_nop 0
	v_addc_co_u32_e32 v1, vcc, 0, v33, vcc
	global_store_dword v[0:1], v2, off sc1
	v_add_f32_e32 v0, v12, v252
	s_mov_b32 s0, 0x60000
	v_fmac_f32_e32 v136, v205, v0
	v_add_co_u32_e32 v0, vcc, s0, v32
	v_mul_f32_e32 v2, v34, v136
	s_nop 0
	v_addc_co_u32_e32 v1, vcc, 0, v33, vcc
	global_store_dword v[0:1], v2, off sc1
	v_add_f32_e32 v0, v13, v253
	s_mov_b32 s0, 0x64000
	v_fmac_f32_e32 v137, v205, v0
	v_add_co_u32_e32 v0, vcc, s0, v32
	v_mul_f32_e32 v2, v34, v137
	s_nop 0
	v_addc_co_u32_e32 v1, vcc, 0, v33, vcc
	global_store_dword v[0:1], v2, off sc1
	v_add_f32_e32 v0, v14, v254
	s_mov_b32 s0, 0x68000
	v_fmac_f32_e32 v138, v205, v0
	v_add_co_u32_e32 v0, vcc, s0, v32
	v_mul_f32_e32 v2, v34, v138
	s_nop 0
	v_addc_co_u32_e32 v1, vcc, 0, v33, vcc
	global_store_dword v[0:1], v2, off sc1
	v_add_f32_e32 v0, v15, v255
	v_fmac_f32_e32 v139, v205, v0
	v_add_co_u32_e32 v0, vcc, 0x6c000, v32
	v_mul_f32_e32 v2, v34, v139
	s_nop 0
	v_addc_co_u32_e32 v1, vcc, 0, v33, vcc
	global_store_dword v[0:1], v2, off sc1
	s_endpgm
